# baseline (speedup 1.0000x reference)
_Z12wprep_kernelPKfS0_S0_PDF16_Pj:
	s_load_dwordx8 s[4:11], s[0:1], 0x0
	s_lshr_b32 s12, s2, 3
	v_lshl_or_b32 v12, s12, 8, v0
	v_lshrrev_b32_e32 v12, 1, v12
	v_lshlrev_b32_e32 v12, 12, v12
	v_lshl_or_b32 v2, s2, 8, v0
	v_cmp_lt_i32_e32 vcc, 31, v2
	s_and_saveexec_b64 s[2:3], vcc
	s_xor_b64 s[2:3], exec, s[2:3]
	v_mov_b32_e32 v3, 0
	s_andn2_saveexec_b64 s[2:3], s[2:3]
	s_cbranch_execz .LBB0_4
	s_load_dwordx2 s[0:1], s[0:1], 0x20
	v_ashrrev_i32_e32 v3, 31, v2
	v_mov_b32_e32 v1, 0
	s_waitcnt lgkmcnt(0)
	v_lshl_add_u64 v[4:5], v[2:3], 2, s[0:1]
	global_store_dword v[4:5], v1, off
.LBB0_4:
	s_or_b64 exec, exec, s[2:3]
	s_mov_b32 s0, 0x8000
	v_and_b32_e32 v1, 0xffff8000, v2
	s_waitcnt lgkmcnt(0)
	v_mov_b32_e32 v4, s8
	v_mov_b32_e32 v5, s6
	v_cmp_eq_u32_e32 vcc, s0, v1
	s_nop 1
	v_cndmask_b32_e32 v1, v4, v5, vcc
	v_mov_b32_e32 v4, s9
	v_mov_b32_e32 v5, s7
	v_cndmask_b32_e32 v4, v4, v5, vcc
	v_mov_b32_e32 v5, s5
	v_cmp_gt_u32_e32 vcc, s0, v2
	s_nop 1
	v_cndmask_b32_e32 v5, v4, v5, vcc
	v_mov_b32_e32 v4, s4
	v_cndmask_b32_e32 v4, v1, v4, vcc
	v_lshrrev_b32_e32 v1, 4, v0
	v_xor_b32_e32 v6, v1, v0
	v_lshlrev_b32_e32 v0, 9, v2
	v_and_b32_e32 v0, 0xff800, v0
	v_mov_b32_e32 v1, 0
	v_lshl_add_u64 v[4:5], v[4:5], 0, v[0:1]
	v_lshrrev_b32_e32 v0, 4, v2
	v_and_b32_e32 v0, 0x780, v0
	v_lshl_add_u64 v[4:5], v[4:5], 0, v[0:1]
	v_lshlrev_b32_e32 v0, 5, v6
	v_and_b32_e32 v0, 0x60, v0
	v_lshl_add_u64 v[0:1], v[4:5], 0, v[0:1]
	global_load_dwordx4 v[4:7], v[0:1], off
	global_load_dwordx4 v[8:11], v[0:1], off offset:16
	v_lshl_add_u64 v[0:1], v[2:3], 4, s[10:11]
	s_waitcnt vmcnt(1)
	v_cvt_pk_f16_f32 v4, v4, v5
	v_cvt_pk_f16_f32 v5, v6, v7
	s_waitcnt vmcnt(0)
	v_cvt_pk_f16_f32 v6, v8, v9
	v_cvt_pk_f16_f32 v7, v10, v11
	global_store_dwordx4 v[0:1], v[4:7], off
	s_sub_u32 s14, s10, 0x1800000
	s_subb_u32 s15, s11, 0
	global_load_dword v13, v12, s[14:15]
	s_endpgm

	.amdhsa_kernel _Z12wprep_kernelPKfS0_S0_PDF16_Pj
		.amdhsa_group_segment_fixed_size 0
		.amdhsa_private_segment_fixed_size 0
		.amdhsa_kernarg_size 40
		.amdhsa_user_sgpr_count 2
		.amdhsa_user_sgpr_dispatch_ptr 0
		.amdhsa_user_sgpr_queue_ptr 0
		.amdhsa_user_sgpr_kernarg_segment_ptr 1
		.amdhsa_user_sgpr_dispatch_id 0
		.amdhsa_user_sgpr_kernarg_preload_length 0
		.amdhsa_user_sgpr_kernarg_preload_offset 0
		.amdhsa_user_sgpr_private_segment_size 0
		.amdhsa_uses_dynamic_stack 0
		.amdhsa_enable_private_segment 0
		.amdhsa_system_sgpr_workgroup_id_x 1
		.amdhsa_system_sgpr_workgroup_id_y 0
		.amdhsa_system_sgpr_workgroup_id_z 0
		.amdhsa_system_sgpr_workgroup_info 0
		.amdhsa_system_vgpr_workitem_id 0
		.amdhsa_next_free_vgpr 16
		.amdhsa_next_free_sgpr 16
		.amdhsa_accum_offset 16
		.amdhsa_reserve_vcc 1
		.amdhsa_float_round_mode_32 0
		.amdhsa_float_round_mode_16_64 0
		.amdhsa_float_denorm_mode_32 3
		.amdhsa_float_denorm_mode_16_64 3
		.amdhsa_dx10_clamp 1
		.amdhsa_ieee_mode 1
		.amdhsa_fp16_overflow 0
		.amdhsa_tg_split 0
		.amdhsa_exception_fp_ieee_invalid_op 0
		.amdhsa_exception_fp_denorm_src 0
		.amdhsa_exception_fp_ieee_div_zero 0
		.amdhsa_exception_fp_ieee_overflow 0
		.amdhsa_exception_fp_ieee_underflow 0
		.amdhsa_exception_fp_ieee_inexact 0
		.amdhsa_exception_int_div_zero 0
	.end_amdhsa_kernel

amdhsa.kernels:
  - .agpr_count:     0
    .args:
      - .actual_access:  read_only
        .address_space:  global
        .offset:         0
        .size:           8
        .value_kind:     global_buffer
      - .actual_access:  read_only
        .address_space:  global
        .offset:         8
        .size:           8
        .value_kind:     global_buffer
      - .actual_access:  read_only
        .address_space:  global
        .offset:         16
        .size:           8
        .value_kind:     global_buffer
      - .actual_access:  write_only
        .address_space:  global
        .offset:         24
        .size:           8
        .value_kind:     global_buffer
      - .actual_access:  write_only
        .address_space:  global
        .offset:         32
        .size:           8
        .value_kind:     global_buffer
    .group_segment_fixed_size: 0
    .kernarg_segment_align: 8
    .kernarg_segment_size: 40
    .language:       OpenCL C
    .language_version:
      - 2
      - 0
    .max_flat_workgroup_size: 256
    .name:           _Z12wprep_kernelPKfS0_S0_PDF16_Pj
    .private_segment_fixed_size: 0
    .sgpr_count:     22
    .sgpr_spill_count: 0
    .symbol:         _Z12wprep_kernelPKfS0_S0_PDF16_Pj.kd
    .uniform_work_group_size: 1
    .uses_dynamic_stack: false
    .vgpr_count:     16
    .vgpr_spill_count: 0
    .wavefront_size: 64
  - .agpr_count:     0
    .args:
      - .actual_access:  read_only
        .address_space:  global
        .offset:         0
        .size:           8
        .value_kind:     global_buffer
      - .actual_access:  read_only
        .address_space:  global
        .offset:         8
        .size:           8
        .value_kind:     global_buffer
      - .actual_access:  read_only
        .address_space:  global
        .offset:         16
        .size:           8
        .value_kind:     global_buffer
      - .actual_access:  read_only
        .address_space:  global
        .offset:         24
        .size:           8
        .value_kind:     global_buffer
      - .actual_access:  read_only
        .address_space:  global
        .offset:         32
        .size:           8
        .value_kind:     global_buffer
      - .actual_access:  read_only
        .address_space:  global
        .offset:         40
        .size:           8
        .value_kind:     global_buffer
      - .actual_access:  read_only
        .address_space:  global
        .offset:         48
        .size:           8
        .value_kind:     global_buffer
      - .actual_access:  write_only
        .address_space:  global
        .offset:         56
        .size:           8
        .value_kind:     global_buffer
      - .actual_access:  write_only
        .address_space:  global
        .offset:         64
        .size:           8
        .value_kind:     global_buffer
      - .actual_access:  write_only
        .address_space:  global
        .offset:         72
        .size:           8
        .value_kind:     global_buffer
      - .address_space:  global
        .offset:         80
        .size:           8
        .value_kind:     global_buffer
    .group_segment_fixed_size: 0
    .kernarg_segment_align: 8
    .kernarg_segment_size: 88
    .language:       OpenCL C
    .language_version:
      - 2
      - 0
    .max_flat_workgroup_size: 512
    .name:           _Z11proj_kernelPKfS0_S0_PKDF16_S0_S0_S0_PDF16_S3_S3_Pj
    .private_segment_fixed_size: 0
    .sgpr_count:     54
    .sgpr_spill_count: 0
    .symbol:         _Z11proj_kernelPKfS0_S0_PKDF16_S0_S0_S0_PDF16_S3_S3_Pj.kd
    .uniform_work_group_size: 1
    .uses_dynamic_stack: false
    .vgpr_count:     256
    .vgpr_spill_count: 0
    .wavefront_size: 64
  - .agpr_count:     0
    .args:
      - .actual_access:  read_only
        .address_space:  global
        .offset:         0
        .size:           8
        .value_kind:     global_buffer
      - .address_space:  global
        .offset:         8
        .size:           8
        .value_kind:     global_buffer
      - .address_space:  global
        .offset:         16
        .size:           8
        .value_kind:     global_buffer
      - .actual_access:  read_only
        .address_space:  global
        .offset:         24
        .size:           8
        .value_kind:     global_buffer
      - .actual_access:  write_only
        .address_space:  global
        .offset:         32
        .size:           8
        .value_kind:     global_buffer
    .group_segment_fixed_size: 0
    .kernarg_segment_align: 8
    .kernarg_segment_size: 40
    .language:       OpenCL C
    .language_version:
      - 2
      - 0
    .max_flat_workgroup_size: 512
    .name:           _Z11attn_kernelPKDF16_S0_S0_PKjPf
    .private_segment_fixed_size: 0
    .sgpr_count:     43
    .sgpr_spill_count: 0
    .symbol:         _Z11attn_kernelPKDF16_S0_S0_PKjPf.kd
    .uniform_work_group_size: 1
    .uses_dynamic_stack: false
    .vgpr_count:     196
    .vgpr_spill_count: 0
    .wavefront_size: 64
